# both Hyena filter instantiations (Lf=SEQ and the 4 Lf=LC units) with the output layer on v_mfma_f32_32x32x2_f32
# speedup vs baseline: 1.0203x; 1.0062x over previous
.LBB0_338:
	s_lshl_b64 s[4:5], s[20:21], 2
	v_readlane_b32 s6, v252, 31
	s_add_u32 s6, s6, s4
	v_readlane_b32 s7, v252, 32
	s_addc_u32 s7, s7, s5
	s_mov_b32 s25, s21
	s_lshl_b64 s[4:5], s[24:25], 2
	v_readlane_b32 s8, v252, 33
	s_add_u32 s8, s8, s4
	v_readlane_b32 s9, v252, 34
	s_addc_u32 s9, s9, s5
	s_lshl_b32 s23, s23, 6
	s_add_i32 s23, s23, 0xffff7f80
	s_load_dwordx2 s[4:5], s[0:1], 0xc8
	s_waitcnt lgkmcnt(0)
	s_mov_b64 exec, -1
	v_lshrrev_b32_e32 v2, 6, v0
	v_and_b32_e32 v3, 63, v0
	v_readfirstlane_b32 s31, v2
	v_lshrrev_b32_e32 v4, 5, v3
	v_and_b32_e32 v5, 31, v3
	s_lshl_b32 s10, s31, 9
	s_add_u32 s24, s4, s10
	s_addc_u32 s25, s5, 0
	s_lshl_b32 s10, s31, 17
	s_add_u32 s26, s6, s10
	s_addc_u32 s27, s7, 0
	s_lshl_b32 s10, s31, 11
	s_add_u32 s28, s8, s10
	s_addc_u32 s29, s9, 0
	v_lshlrev_b32_e32 v6, 2, v5
	v_lshl_add_u32 v8, v4, 17, v6
	v_lshl_add_u32 v9, v4, 12, v6
	v_add_u32_e32 v10, 0x80, v9
	v_lshlrev_b32_e32 v76, 6, v4
	v_add_u32_e32 v6, s23, v5
	v_cvt_f32_i32_e32 v77, v6
	v_mul_f32_e64 v77, |v77|, s94
	v_add_u32_e32 v6, 32, v6
	v_cvt_f32_i32_e32 v158, v6
	v_mul_f32_e64 v158, |v158|, s94
	s_lshl_b32 s10, s31, 7
	v_lshl_add_u32 v6, v4, 2, s10
	v_cvt_f32_i32_e32 v159, v6
	v_mul_u32_u24_e32 v6, 0x110, v5
	v_lshl_add_u32 v160, v4, 7, v6
	v_add_u32_e32 v160, 0x2400, v160
	s_mov_b32 s34, 0x80000000
	s_mov_b32 s35, 0x80000000
	s_mov_b32 s40, s24
	s_mov_b32 s41, s25
	global_load_dword v126, v8, s[40:41]
	s_add_u32 s40, s40, 0x1000
	s_addc_u32 s41, s41, 0
	global_load_dword v127, v8, s[40:41]
	s_add_u32 s40, s40, 0x1000
	s_addc_u32 s41, s41, 0
	global_load_dword v128, v8, s[40:41]
	s_add_u32 s40, s40, 0x1000
	s_addc_u32 s41, s41, 0
	global_load_dword v129, v8, s[40:41]
	s_add_u32 s40, s40, 0x1000
	s_addc_u32 s41, s41, 0
	global_load_dword v130, v8, s[40:41]
	s_add_u32 s40, s40, 0x1000
	s_addc_u32 s41, s41, 0
	global_load_dword v131, v8, s[40:41]
	s_add_u32 s40, s40, 0x1000
	s_addc_u32 s41, s41, 0
	global_load_dword v132, v8, s[40:41]
	s_add_u32 s40, s40, 0x1000
	s_addc_u32 s41, s41, 0
	global_load_dword v133, v8, s[40:41]
	s_add_u32 s40, s40, 0x1000
	s_addc_u32 s41, s41, 0
	global_load_dword v134, v8, s[40:41]
	s_add_u32 s40, s40, 0x1000
	s_addc_u32 s41, s41, 0
	global_load_dword v135, v8, s[40:41]
	s_add_u32 s40, s40, 0x1000
	s_addc_u32 s41, s41, 0
	global_load_dword v136, v8, s[40:41]
	s_add_u32 s40, s40, 0x1000
	s_addc_u32 s41, s41, 0
	global_load_dword v137, v8, s[40:41]
	s_add_u32 s40, s40, 0x1000
	s_addc_u32 s41, s41, 0
	global_load_dword v138, v8, s[40:41]
	s_add_u32 s40, s40, 0x1000
	s_addc_u32 s41, s41, 0
	global_load_dword v139, v8, s[40:41]
	s_add_u32 s40, s40, 0x1000
	s_addc_u32 s41, s41, 0
	global_load_dword v140, v8, s[40:41]
	s_add_u32 s40, s40, 0x1000
	s_addc_u32 s41, s41, 0
	global_load_dword v141, v8, s[40:41]
	s_add_u32 s40, s40, 0x1000
	s_addc_u32 s41, s41, 0
	global_load_dword v142, v8, s[40:41]
	s_add_u32 s40, s40, 0x1000
	s_addc_u32 s41, s41, 0
	global_load_dword v143, v8, s[40:41]
	s_add_u32 s40, s40, 0x1000
	s_addc_u32 s41, s41, 0
	global_load_dword v144, v8, s[40:41]
	s_add_u32 s40, s40, 0x1000
	s_addc_u32 s41, s41, 0
	global_load_dword v145, v8, s[40:41]
	s_add_u32 s40, s40, 0x1000
	s_addc_u32 s41, s41, 0
	global_load_dword v146, v8, s[40:41]
	s_add_u32 s40, s40, 0x1000
	s_addc_u32 s41, s41, 0
	global_load_dword v147, v8, s[40:41]
	s_add_u32 s40, s40, 0x1000
	s_addc_u32 s41, s41, 0
	global_load_dword v148, v8, s[40:41]
	s_add_u32 s40, s40, 0x1000
	s_addc_u32 s41, s41, 0
	global_load_dword v149, v8, s[40:41]
	s_add_u32 s40, s40, 0x1000
	s_addc_u32 s41, s41, 0
	global_load_dword v150, v8, s[40:41]
	s_add_u32 s40, s40, 0x1000
	s_addc_u32 s41, s41, 0
	global_load_dword v151, v8, s[40:41]
	s_add_u32 s40, s40, 0x1000
	s_addc_u32 s41, s41, 0
	global_load_dword v152, v8, s[40:41]
	s_add_u32 s40, s40, 0x1000
	s_addc_u32 s41, s41, 0
	global_load_dword v153, v8, s[40:41]
	s_add_u32 s40, s40, 0x1000
	s_addc_u32 s41, s41, 0
	global_load_dword v154, v8, s[40:41]
	s_add_u32 s40, s40, 0x1000
	s_addc_u32 s41, s41, 0
	global_load_dword v155, v8, s[40:41]
	s_add_u32 s40, s40, 0x1000
	s_addc_u32 s41, s41, 0
	global_load_dword v156, v8, s[40:41]
	s_add_u32 s40, s40, 0x1000
	s_addc_u32 s41, s41, 0
	global_load_dword v157, v8, s[40:41]
	s_add_u32 s40, s40, 0x1000
	s_addc_u32 s41, s41, 0
	s_add_u32 s24, s24, 0x80
	s_addc_u32 s25, s25, 0
	s_waitcnt lgkmcnt(0)
	s_barrier
	ds_read_b128 v[12:15], v160 offset:0
	ds_read_b128 v[44:47], v160 offset:8704
	ds_read_b128 v[16:19], v160 offset:16
	ds_read_b128 v[48:51], v160 offset:8720
	ds_read_b128 v[20:23], v160 offset:32
	ds_read_b128 v[52:55], v160 offset:8736
	ds_read_b128 v[24:27], v160 offset:48
	ds_read_b128 v[56:59], v160 offset:8752
	ds_read_b128 v[28:31], v160 offset:64
	ds_read_b128 v[60:63], v160 offset:8768
	ds_read_b128 v[32:35], v160 offset:80
	ds_read_b128 v[64:67], v160 offset:8784
	ds_read_b128 v[36:39], v160 offset:96
	ds_read_b128 v[68:71], v160 offset:8800
	ds_read_b128 v[40:43], v160 offset:112
	ds_read_b128 v[72:75], v160 offset:8816
	s_mov_b32 s30, 0
	s_waitcnt vmcnt(0) lgkmcnt(0)

.Lhfc_noload:
	s_nop 15
	s_nop 7
	s_mov_b32 s44, s26
	s_mov_b32 s45, s27
	v_add_f32_e32 v2, 0, v159
	v_fmamk_f32 v2, v2, 0x3e2119e2, v80
	v_mul_f32_e64 v3, |v2|, v77
	v_mul_f32_e32 v4, 0x3fb8aa3b, v3
	v_fma_f32 v5, v3, s95, -v4
	v_rndne_f32_e32 v6, v4
	v_fmac_f32_e32 v5, 0x32a5705f, v3
	v_sub_f32_e32 v4, v4, v6
	v_add_f32_e32 v4, v4, v5
	v_exp_f32_e32 v4, v4
	v_cvt_i32_f32_e32 v6, v6
	v_cmp_ngt_f32_e32 vcc, s96, v3
	v_ldexp_f32 v4, v4, v6
	s_nop 0
	v_cndmask_b32_e32 v4, 0, v4, vcc
	v_cmp_nlt_f32_e32 vcc, s97, v3
	s_nop 1
	v_cndmask_b32_e32 v4, v93, v4, vcc
	v_mul_f32_e32 v4, v4, v94
	global_store_dword v9, v4, s[44:45]
	v_mul_f32_e64 v3, |v2|, v158
	v_mul_f32_e32 v7, 0x3fb8aa3b, v3
	v_fma_f32 v5, v3, s95, -v7
	v_rndne_f32_e32 v6, v7
	v_fmac_f32_e32 v5, 0x32a5705f, v3
	v_sub_f32_e32 v7, v7, v6
	v_add_f32_e32 v7, v7, v5
	v_exp_f32_e32 v7, v7
	v_cvt_i32_f32_e32 v6, v6
	v_cmp_ngt_f32_e32 vcc, s96, v3
	v_ldexp_f32 v7, v7, v6
	s_nop 0
	v_cndmask_b32_e32 v7, 0, v7, vcc
	v_cmp_nlt_f32_e32 vcc, s97, v3
	s_nop 1
	v_cndmask_b32_e32 v7, v93, v7, vcc
	v_mul_f32_e32 v7, v7, v110
	global_store_dword v10, v7, s[44:45]
	v_add_f32_e64 v94, |v4|, |v7|
	s_add_u32 s44, s44, 0x400
	s_addc_u32 s45, s45, 0
	v_add_f32_e32 v2, 0x3f800000, v159
	v_fmamk_f32 v2, v2, 0x3e2119e2, v80
	v_mul_f32_e64 v3, |v2|, v77
	v_mul_f32_e32 v4, 0x3fb8aa3b, v3
	v_fma_f32 v5, v3, s95, -v4
	v_rndne_f32_e32 v6, v4
	v_fmac_f32_e32 v5, 0x32a5705f, v3
	v_sub_f32_e32 v4, v4, v6
	v_add_f32_e32 v4, v4, v5
	v_exp_f32_e32 v4, v4
	v_cvt_i32_f32_e32 v6, v6
	v_cmp_ngt_f32_e32 vcc, s96, v3
	v_ldexp_f32 v4, v4, v6
	s_nop 0
	v_cndmask_b32_e32 v4, 0, v4, vcc
	v_cmp_nlt_f32_e32 vcc, s97, v3
	s_nop 1
	v_cndmask_b32_e32 v4, v93, v4, vcc
	v_mul_f32_e32 v4, v4, v95
	global_store_dword v9, v4, s[44:45]
	v_mul_f32_e64 v3, |v2|, v158
	v_mul_f32_e32 v7, 0x3fb8aa3b, v3
	v_fma_f32 v5, v3, s95, -v7
	v_rndne_f32_e32 v6, v7
	v_fmac_f32_e32 v5, 0x32a5705f, v3
	v_sub_f32_e32 v7, v7, v6
	v_add_f32_e32 v7, v7, v5
	v_exp_f32_e32 v7, v7
	v_cvt_i32_f32_e32 v6, v6
	v_cmp_ngt_f32_e32 vcc, s96, v3
	v_ldexp_f32 v7, v7, v6
	s_nop 0
	v_cndmask_b32_e32 v7, 0, v7, vcc
	v_cmp_nlt_f32_e32 vcc, s97, v3
	s_nop 1
	v_cndmask_b32_e32 v7, v93, v7, vcc
	v_mul_f32_e32 v7, v7, v111
	global_store_dword v10, v7, s[44:45]
	v_add_f32_e64 v95, |v4|, |v7|
	s_add_u32 s44, s44, 0x400
	s_addc_u32 s45, s45, 0
	v_add_f32_e32 v2, 0x40000000, v159
	v_fmamk_f32 v2, v2, 0x3e2119e2, v80
	v_mul_f32_e64 v3, |v2|, v77
	v_mul_f32_e32 v4, 0x3fb8aa3b, v3
	v_fma_f32 v5, v3, s95, -v4
	v_rndne_f32_e32 v6, v4
	v_fmac_f32_e32 v5, 0x32a5705f, v3
	v_sub_f32_e32 v4, v4, v6
	v_add_f32_e32 v4, v4, v5
	v_exp_f32_e32 v4, v4
	v_cvt_i32_f32_e32 v6, v6
	v_cmp_ngt_f32_e32 vcc, s96, v3
	v_ldexp_f32 v4, v4, v6
	s_nop 0
	v_cndmask_b32_e32 v4, 0, v4, vcc
	v_cmp_nlt_f32_e32 vcc, s97, v3
	s_nop 1
	v_cndmask_b32_e32 v4, v93, v4, vcc
	v_mul_f32_e32 v4, v4, v96
	global_store_dword v9, v4, s[44:45]
	v_mul_f32_e64 v3, |v2|, v158
	v_mul_f32_e32 v7, 0x3fb8aa3b, v3
	v_fma_f32 v5, v3, s95, -v7
	v_rndne_f32_e32 v6, v7
	v_fmac_f32_e32 v5, 0x32a5705f, v3
	v_sub_f32_e32 v7, v7, v6
	v_add_f32_e32 v7, v7, v5
	v_exp_f32_e32 v7, v7
	v_cvt_i32_f32_e32 v6, v6
	v_cmp_ngt_f32_e32 vcc, s96, v3
	v_ldexp_f32 v7, v7, v6
	s_nop 0
	v_cndmask_b32_e32 v7, 0, v7, vcc
	v_cmp_nlt_f32_e32 vcc, s97, v3
	s_nop 1
	v_cndmask_b32_e32 v7, v93, v7, vcc
	v_mul_f32_e32 v7, v7, v112
	global_store_dword v10, v7, s[44:45]
	v_add_f32_e64 v96, |v4|, |v7|
	s_add_u32 s44, s44, 0x400
	s_addc_u32 s45, s45, 0
	v_add_f32_e32 v2, 0x40400000, v159
	v_fmamk_f32 v2, v2, 0x3e2119e2, v80
	v_mul_f32_e64 v3, |v2|, v77
	v_mul_f32_e32 v4, 0x3fb8aa3b, v3
	v_fma_f32 v5, v3, s95, -v4
	v_rndne_f32_e32 v6, v4
	v_fmac_f32_e32 v5, 0x32a5705f, v3
	v_sub_f32_e32 v4, v4, v6
	v_add_f32_e32 v4, v4, v5
	v_exp_f32_e32 v4, v4
	v_cvt_i32_f32_e32 v6, v6
	v_cmp_ngt_f32_e32 vcc, s96, v3
	v_ldexp_f32 v4, v4, v6
	s_nop 0
	v_cndmask_b32_e32 v4, 0, v4, vcc
	v_cmp_nlt_f32_e32 vcc, s97, v3
	s_nop 1
	v_cndmask_b32_e32 v4, v93, v4, vcc
	v_mul_f32_e32 v4, v4, v97
	global_store_dword v9, v4, s[44:45]
	v_mul_f32_e64 v3, |v2|, v158
	v_mul_f32_e32 v7, 0x3fb8aa3b, v3
	v_fma_f32 v5, v3, s95, -v7
	v_rndne_f32_e32 v6, v7
	v_fmac_f32_e32 v5, 0x32a5705f, v3
	v_sub_f32_e32 v7, v7, v6
	v_add_f32_e32 v7, v7, v5
	v_exp_f32_e32 v7, v7
	v_cvt_i32_f32_e32 v6, v6
	v_cmp_ngt_f32_e32 vcc, s96, v3
	v_ldexp_f32 v7, v7, v6
	s_nop 0
	v_cndmask_b32_e32 v7, 0, v7, vcc
	v_cmp_nlt_f32_e32 vcc, s97, v3
	s_nop 1
	v_cndmask_b32_e32 v7, v93, v7, vcc
	v_mul_f32_e32 v7, v7, v113
	global_store_dword v10, v7, s[44:45]
	v_add_f32_e64 v97, |v4|, |v7|
	s_add_u32 s44, s44, 0x1400
	s_addc_u32 s45, s45, 0
	v_add_f32_e32 v2, 0x41000000, v159
	v_fmamk_f32 v2, v2, 0x3e2119e2, v80
	v_mul_f32_e64 v3, |v2|, v77
	v_mul_f32_e32 v4, 0x3fb8aa3b, v3
	v_fma_f32 v5, v3, s95, -v4
	v_rndne_f32_e32 v6, v4
	v_fmac_f32_e32 v5, 0x32a5705f, v3
	v_sub_f32_e32 v4, v4, v6
	v_add_f32_e32 v4, v4, v5
	v_exp_f32_e32 v4, v4
	v_cvt_i32_f32_e32 v6, v6
	v_cmp_ngt_f32_e32 vcc, s96, v3
	v_ldexp_f32 v4, v4, v6
	s_nop 0
	v_cndmask_b32_e32 v4, 0, v4, vcc
	v_cmp_nlt_f32_e32 vcc, s97, v3
	s_nop 1
	v_cndmask_b32_e32 v4, v93, v4, vcc
	v_mul_f32_e32 v4, v4, v98
	global_store_dword v9, v4, s[44:45]
	v_mul_f32_e64 v3, |v2|, v158
	v_mul_f32_e32 v7, 0x3fb8aa3b, v3
	v_fma_f32 v5, v3, s95, -v7
	v_rndne_f32_e32 v6, v7
	v_fmac_f32_e32 v5, 0x32a5705f, v3
	v_sub_f32_e32 v7, v7, v6
	v_add_f32_e32 v7, v7, v5
	v_exp_f32_e32 v7, v7
	v_cvt_i32_f32_e32 v6, v6
	v_cmp_ngt_f32_e32 vcc, s96, v3
	v_ldexp_f32 v7, v7, v6
	s_nop 0
	v_cndmask_b32_e32 v7, 0, v7, vcc
	v_cmp_nlt_f32_e32 vcc, s97, v3
	s_nop 1
	v_cndmask_b32_e32 v7, v93, v7, vcc
	v_mul_f32_e32 v7, v7, v114
	global_store_dword v10, v7, s[44:45]
	v_add_f32_e64 v98, |v4|, |v7|
	s_add_u32 s44, s44, 0x400
	s_addc_u32 s45, s45, 0
	v_add_f32_e32 v2, 0x41100000, v159
	v_fmamk_f32 v2, v2, 0x3e2119e2, v80
	v_mul_f32_e64 v3, |v2|, v77
	v_mul_f32_e32 v4, 0x3fb8aa3b, v3
	v_fma_f32 v5, v3, s95, -v4
	v_rndne_f32_e32 v6, v4
	v_fmac_f32_e32 v5, 0x32a5705f, v3
	v_sub_f32_e32 v4, v4, v6
	v_add_f32_e32 v4, v4, v5
	v_exp_f32_e32 v4, v4
	v_cvt_i32_f32_e32 v6, v6
	v_cmp_ngt_f32_e32 vcc, s96, v3
	v_ldexp_f32 v4, v4, v6
	s_nop 0
	v_cndmask_b32_e32 v4, 0, v4, vcc
	v_cmp_nlt_f32_e32 vcc, s97, v3
	s_nop 1
	v_cndmask_b32_e32 v4, v93, v4, vcc
	v_mul_f32_e32 v4, v4, v99
	global_store_dword v9, v4, s[44:45]
	v_mul_f32_e64 v3, |v2|, v158
	v_mul_f32_e32 v7, 0x3fb8aa3b, v3
	v_fma_f32 v5, v3, s95, -v7
	v_rndne_f32_e32 v6, v7
	v_fmac_f32_e32 v5, 0x32a5705f, v3
	v_sub_f32_e32 v7, v7, v6
	v_add_f32_e32 v7, v7, v5
	v_exp_f32_e32 v7, v7
	v_cvt_i32_f32_e32 v6, v6
	v_cmp_ngt_f32_e32 vcc, s96, v3
	v_ldexp_f32 v7, v7, v6
	s_nop 0
	v_cndmask_b32_e32 v7, 0, v7, vcc
	v_cmp_nlt_f32_e32 vcc, s97, v3
	s_nop 1
	v_cndmask_b32_e32 v7, v93, v7, vcc
	v_mul_f32_e32 v7, v7, v115
	global_store_dword v10, v7, s[44:45]
	v_add_f32_e64 v99, |v4|, |v7|
	s_add_u32 s44, s44, 0x400
	s_addc_u32 s45, s45, 0
	v_add_f32_e32 v2, 0x41200000, v159
	v_fmamk_f32 v2, v2, 0x3e2119e2, v80
	v_mul_f32_e64 v3, |v2|, v77
	v_mul_f32_e32 v4, 0x3fb8aa3b, v3
	v_fma_f32 v5, v3, s95, -v4
	v_rndne_f32_e32 v6, v4
	v_fmac_f32_e32 v5, 0x32a5705f, v3
	v_sub_f32_e32 v4, v4, v6
	v_add_f32_e32 v4, v4, v5
	v_exp_f32_e32 v4, v4
	v_cvt_i32_f32_e32 v6, v6
	v_cmp_ngt_f32_e32 vcc, s96, v3
	v_ldexp_f32 v4, v4, v6
	s_nop 0
	v_cndmask_b32_e32 v4, 0, v4, vcc
	v_cmp_nlt_f32_e32 vcc, s97, v3
	s_nop 1
	v_cndmask_b32_e32 v4, v93, v4, vcc
	v_mul_f32_e32 v4, v4, v100
	global_store_dword v9, v4, s[44:45]
	v_mul_f32_e64 v3, |v2|, v158
	v_mul_f32_e32 v7, 0x3fb8aa3b, v3
	v_fma_f32 v5, v3, s95, -v7
	v_rndne_f32_e32 v6, v7
	v_fmac_f32_e32 v5, 0x32a5705f, v3
	v_sub_f32_e32 v7, v7, v6
	v_add_f32_e32 v7, v7, v5
	v_exp_f32_e32 v7, v7
	v_cvt_i32_f32_e32 v6, v6
	v_cmp_ngt_f32_e32 vcc, s96, v3
	v_ldexp_f32 v7, v7, v6
	s_nop 0
	v_cndmask_b32_e32 v7, 0, v7, vcc
	v_cmp_nlt_f32_e32 vcc, s97, v3
	s_nop 1
	v_cndmask_b32_e32 v7, v93, v7, vcc
	v_mul_f32_e32 v7, v7, v116
	global_store_dword v10, v7, s[44:45]
	v_add_f32_e64 v100, |v4|, |v7|
	s_add_u32 s44, s44, 0x400
	s_addc_u32 s45, s45, 0
	v_add_f32_e32 v2, 0x41300000, v159
	v_fmamk_f32 v2, v2, 0x3e2119e2, v80
	v_mul_f32_e64 v3, |v2|, v77
	v_mul_f32_e32 v4, 0x3fb8aa3b, v3
	v_fma_f32 v5, v3, s95, -v4
	v_rndne_f32_e32 v6, v4
	v_fmac_f32_e32 v5, 0x32a5705f, v3
	v_sub_f32_e32 v4, v4, v6
	v_add_f32_e32 v4, v4, v5
	v_exp_f32_e32 v4, v4
	v_cvt_i32_f32_e32 v6, v6
	v_cmp_ngt_f32_e32 vcc, s96, v3
	v_ldexp_f32 v4, v4, v6
	s_nop 0
	v_cndmask_b32_e32 v4, 0, v4, vcc
	v_cmp_nlt_f32_e32 vcc, s97, v3
	s_nop 1
	v_cndmask_b32_e32 v4, v93, v4, vcc
	v_mul_f32_e32 v4, v4, v101
	global_store_dword v9, v4, s[44:45]
	v_mul_f32_e64 v3, |v2|, v158
	v_mul_f32_e32 v7, 0x3fb8aa3b, v3
	v_fma_f32 v5, v3, s95, -v7
	v_rndne_f32_e32 v6, v7
	v_fmac_f32_e32 v5, 0x32a5705f, v3
	v_sub_f32_e32 v7, v7, v6
	v_add_f32_e32 v7, v7, v5
	v_exp_f32_e32 v7, v7
	v_cvt_i32_f32_e32 v6, v6
	v_cmp_ngt_f32_e32 vcc, s96, v3
	v_ldexp_f32 v7, v7, v6
	s_nop 0
	v_cndmask_b32_e32 v7, 0, v7, vcc
	v_cmp_nlt_f32_e32 vcc, s97, v3
	s_nop 1
	v_cndmask_b32_e32 v7, v93, v7, vcc
	v_mul_f32_e32 v7, v7, v117
	global_store_dword v10, v7, s[44:45]
	v_add_f32_e64 v101, |v4|, |v7|
	s_add_u32 s44, s44, 0x1400
	s_addc_u32 s45, s45, 0
	v_add_f32_e32 v2, 0x41800000, v159
	v_fmamk_f32 v2, v2, 0x3e2119e2, v80
	v_mul_f32_e64 v3, |v2|, v77
	v_mul_f32_e32 v4, 0x3fb8aa3b, v3
	v_fma_f32 v5, v3, s95, -v4
	v_rndne_f32_e32 v6, v4
	v_fmac_f32_e32 v5, 0x32a5705f, v3
	v_sub_f32_e32 v4, v4, v6
	v_add_f32_e32 v4, v4, v5
	v_exp_f32_e32 v4, v4
	v_cvt_i32_f32_e32 v6, v6
	v_cmp_ngt_f32_e32 vcc, s96, v3
	v_ldexp_f32 v4, v4, v6
	s_nop 0
	v_cndmask_b32_e32 v4, 0, v4, vcc
	v_cmp_nlt_f32_e32 vcc, s97, v3
	s_nop 1
	v_cndmask_b32_e32 v4, v93, v4, vcc
	v_mul_f32_e32 v4, v4, v102
	global_store_dword v9, v4, s[44:45]
	v_mul_f32_e64 v3, |v2|, v158
	v_mul_f32_e32 v7, 0x3fb8aa3b, v3
	v_fma_f32 v5, v3, s95, -v7
	v_rndne_f32_e32 v6, v7
	v_fmac_f32_e32 v5, 0x32a5705f, v3
	v_sub_f32_e32 v7, v7, v6
	v_add_f32_e32 v7, v7, v5
	v_exp_f32_e32 v7, v7
	v_cvt_i32_f32_e32 v6, v6
	v_cmp_ngt_f32_e32 vcc, s96, v3
	v_ldexp_f32 v7, v7, v6
	s_nop 0
	v_cndmask_b32_e32 v7, 0, v7, vcc
	v_cmp_nlt_f32_e32 vcc, s97, v3
	s_nop 1
	v_cndmask_b32_e32 v7, v93, v7, vcc
	v_mul_f32_e32 v7, v7, v118
	global_store_dword v10, v7, s[44:45]
	v_add_f32_e64 v102, |v4|, |v7|
	s_add_u32 s44, s44, 0x400
	s_addc_u32 s45, s45, 0
	v_add_f32_e32 v2, 0x41880000, v159
	v_fmamk_f32 v2, v2, 0x3e2119e2, v80
	v_mul_f32_e64 v3, |v2|, v77
	v_mul_f32_e32 v4, 0x3fb8aa3b, v3
	v_fma_f32 v5, v3, s95, -v4
	v_rndne_f32_e32 v6, v4
	v_fmac_f32_e32 v5, 0x32a5705f, v3
	v_sub_f32_e32 v4, v4, v6
	v_add_f32_e32 v4, v4, v5
	v_exp_f32_e32 v4, v4
	v_cvt_i32_f32_e32 v6, v6
	v_cmp_ngt_f32_e32 vcc, s96, v3
	v_ldexp_f32 v4, v4, v6
	s_nop 0
	v_cndmask_b32_e32 v4, 0, v4, vcc
	v_cmp_nlt_f32_e32 vcc, s97, v3
	s_nop 1
	v_cndmask_b32_e32 v4, v93, v4, vcc
	v_mul_f32_e32 v4, v4, v103
	global_store_dword v9, v4, s[44:45]
	v_mul_f32_e64 v3, |v2|, v158
	v_mul_f32_e32 v7, 0x3fb8aa3b, v3
	v_fma_f32 v5, v3, s95, -v7
	v_rndne_f32_e32 v6, v7
	v_fmac_f32_e32 v5, 0x32a5705f, v3
	v_sub_f32_e32 v7, v7, v6
	v_add_f32_e32 v7, v7, v5
	v_exp_f32_e32 v7, v7
	v_cvt_i32_f32_e32 v6, v6
	v_cmp_ngt_f32_e32 vcc, s96, v3
	v_ldexp_f32 v7, v7, v6
	s_nop 0
	v_cndmask_b32_e32 v7, 0, v7, vcc
	v_cmp_nlt_f32_e32 vcc, s97, v3
	s_nop 1
	v_cndmask_b32_e32 v7, v93, v7, vcc
	v_mul_f32_e32 v7, v7, v119
	global_store_dword v10, v7, s[44:45]
	v_add_f32_e64 v103, |v4|, |v7|
	s_add_u32 s44, s44, 0x400
	s_addc_u32 s45, s45, 0
	v_add_f32_e32 v2, 0x41900000, v159
	v_fmamk_f32 v2, v2, 0x3e2119e2, v80
	v_mul_f32_e64 v3, |v2|, v77
	v_mul_f32_e32 v4, 0x3fb8aa3b, v3
	v_fma_f32 v5, v3, s95, -v4
	v_rndne_f32_e32 v6, v4
	v_fmac_f32_e32 v5, 0x32a5705f, v3
	v_sub_f32_e32 v4, v4, v6
	v_add_f32_e32 v4, v4, v5
	v_exp_f32_e32 v4, v4
	v_cvt_i32_f32_e32 v6, v6
	v_cmp_ngt_f32_e32 vcc, s96, v3
	v_ldexp_f32 v4, v4, v6
	s_nop 0
	v_cndmask_b32_e32 v4, 0, v4, vcc
	v_cmp_nlt_f32_e32 vcc, s97, v3
	s_nop 1
	v_cndmask_b32_e32 v4, v93, v4, vcc
	v_mul_f32_e32 v4, v4, v104
	global_store_dword v9, v4, s[44:45]
	v_mul_f32_e64 v3, |v2|, v158
	v_mul_f32_e32 v7, 0x3fb8aa3b, v3
	v_fma_f32 v5, v3, s95, -v7
	v_rndne_f32_e32 v6, v7
	v_fmac_f32_e32 v5, 0x32a5705f, v3
	v_sub_f32_e32 v7, v7, v6
	v_add_f32_e32 v7, v7, v5
	v_exp_f32_e32 v7, v7
	v_cvt_i32_f32_e32 v6, v6
	v_cmp_ngt_f32_e32 vcc, s96, v3
	v_ldexp_f32 v7, v7, v6
	s_nop 0
	v_cndmask_b32_e32 v7, 0, v7, vcc
	v_cmp_nlt_f32_e32 vcc, s97, v3
	s_nop 1
	v_cndmask_b32_e32 v7, v93, v7, vcc
	v_mul_f32_e32 v7, v7, v120
	global_store_dword v10, v7, s[44:45]
	v_add_f32_e64 v104, |v4|, |v7|
	s_add_u32 s44, s44, 0x400
	s_addc_u32 s45, s45, 0
	v_add_f32_e32 v2, 0x41980000, v159
	v_fmamk_f32 v2, v2, 0x3e2119e2, v80
	v_mul_f32_e64 v3, |v2|, v77
	v_mul_f32_e32 v4, 0x3fb8aa3b, v3
	v_fma_f32 v5, v3, s95, -v4
	v_rndne_f32_e32 v6, v4
	v_fmac_f32_e32 v5, 0x32a5705f, v3
	v_sub_f32_e32 v4, v4, v6
	v_add_f32_e32 v4, v4, v5
	v_exp_f32_e32 v4, v4
	v_cvt_i32_f32_e32 v6, v6
	v_cmp_ngt_f32_e32 vcc, s96, v3
	v_ldexp_f32 v4, v4, v6
	s_nop 0
	v_cndmask_b32_e32 v4, 0, v4, vcc
	v_cmp_nlt_f32_e32 vcc, s97, v3
	s_nop 1
	v_cndmask_b32_e32 v4, v93, v4, vcc
	v_mul_f32_e32 v4, v4, v105
	global_store_dword v9, v4, s[44:45]
	v_mul_f32_e64 v3, |v2|, v158
	v_mul_f32_e32 v7, 0x3fb8aa3b, v3
	v_fma_f32 v5, v3, s95, -v7
	v_rndne_f32_e32 v6, v7
	v_fmac_f32_e32 v5, 0x32a5705f, v3
	v_sub_f32_e32 v7, v7, v6
	v_add_f32_e32 v7, v7, v5
	v_exp_f32_e32 v7, v7
	v_cvt_i32_f32_e32 v6, v6
	v_cmp_ngt_f32_e32 vcc, s96, v3
	v_ldexp_f32 v7, v7, v6
	s_nop 0
	v_cndmask_b32_e32 v7, 0, v7, vcc
	v_cmp_nlt_f32_e32 vcc, s97, v3
	s_nop 1
	v_cndmask_b32_e32 v7, v93, v7, vcc
	v_mul_f32_e32 v7, v7, v121
	global_store_dword v10, v7, s[44:45]
	v_add_f32_e64 v105, |v4|, |v7|
	s_add_u32 s44, s44, 0x1400
	s_addc_u32 s45, s45, 0
	v_add_f32_e32 v2, 0x41c00000, v159
	v_fmamk_f32 v2, v2, 0x3e2119e2, v80
	v_mul_f32_e64 v3, |v2|, v77
	v_mul_f32_e32 v4, 0x3fb8aa3b, v3
	v_fma_f32 v5, v3, s95, -v4
	v_rndne_f32_e32 v6, v4
	v_fmac_f32_e32 v5, 0x32a5705f, v3
	v_sub_f32_e32 v4, v4, v6
	v_add_f32_e32 v4, v4, v5
	v_exp_f32_e32 v4, v4
	v_cvt_i32_f32_e32 v6, v6
	v_cmp_ngt_f32_e32 vcc, s96, v3
	v_ldexp_f32 v4, v4, v6
	s_nop 0
	v_cndmask_b32_e32 v4, 0, v4, vcc
	v_cmp_nlt_f32_e32 vcc, s97, v3
	s_nop 1
	v_cndmask_b32_e32 v4, v93, v4, vcc
	v_mul_f32_e32 v4, v4, v106
	global_store_dword v9, v4, s[44:45]
	v_mul_f32_e64 v3, |v2|, v158
	v_mul_f32_e32 v7, 0x3fb8aa3b, v3
	v_fma_f32 v5, v3, s95, -v7
	v_rndne_f32_e32 v6, v7
	v_fmac_f32_e32 v5, 0x32a5705f, v3
	v_sub_f32_e32 v7, v7, v6
	v_add_f32_e32 v7, v7, v5
	v_exp_f32_e32 v7, v7
	v_cvt_i32_f32_e32 v6, v6
	v_cmp_ngt_f32_e32 vcc, s96, v3
	v_ldexp_f32 v7, v7, v6
	s_nop 0
	v_cndmask_b32_e32 v7, 0, v7, vcc
	v_cmp_nlt_f32_e32 vcc, s97, v3
	s_nop 1
	v_cndmask_b32_e32 v7, v93, v7, vcc
	v_mul_f32_e32 v7, v7, v122
	global_store_dword v10, v7, s[44:45]
	v_add_f32_e64 v106, |v4|, |v7|
	s_add_u32 s44, s44, 0x400
	s_addc_u32 s45, s45, 0
	v_add_f32_e32 v2, 0x41c80000, v159
	v_fmamk_f32 v2, v2, 0x3e2119e2, v80
	v_mul_f32_e64 v3, |v2|, v77
	v_mul_f32_e32 v4, 0x3fb8aa3b, v3
	v_fma_f32 v5, v3, s95, -v4
	v_rndne_f32_e32 v6, v4
	v_fmac_f32_e32 v5, 0x32a5705f, v3
	v_sub_f32_e32 v4, v4, v6
	v_add_f32_e32 v4, v4, v5
	v_exp_f32_e32 v4, v4
	v_cvt_i32_f32_e32 v6, v6
	v_cmp_ngt_f32_e32 vcc, s96, v3
	v_ldexp_f32 v4, v4, v6
	s_nop 0
	v_cndmask_b32_e32 v4, 0, v4, vcc
	v_cmp_nlt_f32_e32 vcc, s97, v3
	s_nop 1
	v_cndmask_b32_e32 v4, v93, v4, vcc
	v_mul_f32_e32 v4, v4, v107
	global_store_dword v9, v4, s[44:45]
	v_mul_f32_e64 v3, |v2|, v158
	v_mul_f32_e32 v7, 0x3fb8aa3b, v3
	v_fma_f32 v5, v3, s95, -v7
	v_rndne_f32_e32 v6, v7
	v_fmac_f32_e32 v5, 0x32a5705f, v3
	v_sub_f32_e32 v7, v7, v6
	v_add_f32_e32 v7, v7, v5
	v_exp_f32_e32 v7, v7
	v_cvt_i32_f32_e32 v6, v6
	v_cmp_ngt_f32_e32 vcc, s96, v3
	v_ldexp_f32 v7, v7, v6
	s_nop 0
	v_cndmask_b32_e32 v7, 0, v7, vcc
	v_cmp_nlt_f32_e32 vcc, s97, v3
	s_nop 1
	v_cndmask_b32_e32 v7, v93, v7, vcc
	v_mul_f32_e32 v7, v7, v123
	global_store_dword v10, v7, s[44:45]
	v_add_f32_e64 v107, |v4|, |v7|
	s_add_u32 s44, s44, 0x400
	s_addc_u32 s45, s45, 0
	v_add_f32_e32 v2, 0x41d00000, v159
	v_fmamk_f32 v2, v2, 0x3e2119e2, v80
	v_mul_f32_e64 v3, |v2|, v77
	v_mul_f32_e32 v4, 0x3fb8aa3b, v3
	v_fma_f32 v5, v3, s95, -v4
	v_rndne_f32_e32 v6, v4
	v_fmac_f32_e32 v5, 0x32a5705f, v3
	v_sub_f32_e32 v4, v4, v6
	v_add_f32_e32 v4, v4, v5
	v_exp_f32_e32 v4, v4
	v_cvt_i32_f32_e32 v6, v6
	v_cmp_ngt_f32_e32 vcc, s96, v3
	v_ldexp_f32 v4, v4, v6
	s_nop 0
	v_cndmask_b32_e32 v4, 0, v4, vcc
	v_cmp_nlt_f32_e32 vcc, s97, v3
	s_nop 1
	v_cndmask_b32_e32 v4, v93, v4, vcc
	v_mul_f32_e32 v4, v4, v108
	global_store_dword v9, v4, s[44:45]
	v_mul_f32_e64 v3, |v2|, v158
	v_mul_f32_e32 v7, 0x3fb8aa3b, v3
	v_fma_f32 v5, v3, s95, -v7
	v_rndne_f32_e32 v6, v7
	v_fmac_f32_e32 v5, 0x32a5705f, v3
	v_sub_f32_e32 v7, v7, v6
	v_add_f32_e32 v7, v7, v5
	v_exp_f32_e32 v7, v7
	v_cvt_i32_f32_e32 v6, v6
	v_cmp_ngt_f32_e32 vcc, s96, v3
	v_ldexp_f32 v7, v7, v6
	s_nop 0
	v_cndmask_b32_e32 v7, 0, v7, vcc
	v_cmp_nlt_f32_e32 vcc, s97, v3
	s_nop 1
	v_cndmask_b32_e32 v7, v93, v7, vcc
	v_mul_f32_e32 v7, v7, v124
	global_store_dword v10, v7, s[44:45]
	v_add_f32_e64 v108, |v4|, |v7|
	s_add_u32 s44, s44, 0x400
	s_addc_u32 s45, s45, 0
	v_add_f32_e32 v2, 0x41d80000, v159
	v_fmamk_f32 v2, v2, 0x3e2119e2, v80
	v_mul_f32_e64 v3, |v2|, v77
	v_mul_f32_e32 v4, 0x3fb8aa3b, v3
	v_fma_f32 v5, v3, s95, -v4
	v_rndne_f32_e32 v6, v4
	v_fmac_f32_e32 v5, 0x32a5705f, v3
	v_sub_f32_e32 v4, v4, v6
	v_add_f32_e32 v4, v4, v5
	v_exp_f32_e32 v4, v4
	v_cvt_i32_f32_e32 v6, v6
	v_cmp_ngt_f32_e32 vcc, s96, v3
	v_ldexp_f32 v4, v4, v6
	s_nop 0
	v_cndmask_b32_e32 v4, 0, v4, vcc
	v_cmp_nlt_f32_e32 vcc, s97, v3
	s_nop 1
	v_cndmask_b32_e32 v4, v93, v4, vcc
	v_mul_f32_e32 v4, v4, v109
	global_store_dword v9, v4, s[44:45]
	v_mul_f32_e64 v3, |v2|, v158
	v_mul_f32_e32 v7, 0x3fb8aa3b, v3
	v_fma_f32 v5, v3, s95, -v7
	v_rndne_f32_e32 v6, v7
	v_fmac_f32_e32 v5, 0x32a5705f, v3
	v_sub_f32_e32 v7, v7, v6
	v_add_f32_e32 v7, v7, v5
	v_exp_f32_e32 v7, v7
	v_cvt_i32_f32_e32 v6, v6
	v_cmp_ngt_f32_e32 vcc, s96, v3
	v_ldexp_f32 v7, v7, v6
	s_nop 0
	v_cndmask_b32_e32 v7, 0, v7, vcc
	v_cmp_nlt_f32_e32 vcc, s97, v3
	s_nop 1
	v_cndmask_b32_e32 v7, v93, v7, vcc
	v_mul_f32_e32 v7, v7, v125
	global_store_dword v10, v7, s[44:45]
	v_add_f32_e64 v109, |v4|, |v7|
	v_add_f32_dpp v94, v94, v94 row_shr:1 row_mask:0xf bank_mask:0xf
	v_add_f32_dpp v95, v95, v95 row_shr:1 row_mask:0xf bank_mask:0xf
	v_add_f32_dpp v96, v96, v96 row_shr:1 row_mask:0xf bank_mask:0xf
	v_add_f32_dpp v97, v97, v97 row_shr:1 row_mask:0xf bank_mask:0xf
	v_add_f32_dpp v98, v98, v98 row_shr:1 row_mask:0xf bank_mask:0xf
	v_add_f32_dpp v99, v99, v99 row_shr:1 row_mask:0xf bank_mask:0xf
	v_add_f32_dpp v100, v100, v100 row_shr:1 row_mask:0xf bank_mask:0xf
	v_add_f32_dpp v101, v101, v101 row_shr:1 row_mask:0xf bank_mask:0xf
	v_add_f32_dpp v102, v102, v102 row_shr:1 row_mask:0xf bank_mask:0xf
	v_add_f32_dpp v103, v103, v103 row_shr:1 row_mask:0xf bank_mask:0xf
	v_add_f32_dpp v104, v104, v104 row_shr:1 row_mask:0xf bank_mask:0xf
	v_add_f32_dpp v105, v105, v105 row_shr:1 row_mask:0xf bank_mask:0xf
	v_add_f32_dpp v106, v106, v106 row_shr:1 row_mask:0xf bank_mask:0xf
	v_add_f32_dpp v107, v107, v107 row_shr:1 row_mask:0xf bank_mask:0xf
	v_add_f32_dpp v108, v108, v108 row_shr:1 row_mask:0xf bank_mask:0xf
	v_add_f32_dpp v109, v109, v109 row_shr:1 row_mask:0xf bank_mask:0xf
	v_add_f32_dpp v94, v94, v94 row_shr:2 row_mask:0xf bank_mask:0xf
	v_add_f32_dpp v95, v95, v95 row_shr:2 row_mask:0xf bank_mask:0xf
	v_add_f32_dpp v96, v96, v96 row_shr:2 row_mask:0xf bank_mask:0xf
	v_add_f32_dpp v97, v97, v97 row_shr:2 row_mask:0xf bank_mask:0xf
	v_add_f32_dpp v98, v98, v98 row_shr:2 row_mask:0xf bank_mask:0xf
	v_add_f32_dpp v99, v99, v99 row_shr:2 row_mask:0xf bank_mask:0xf
	v_add_f32_dpp v100, v100, v100 row_shr:2 row_mask:0xf bank_mask:0xf
	v_add_f32_dpp v101, v101, v101 row_shr:2 row_mask:0xf bank_mask:0xf
	v_add_f32_dpp v102, v102, v102 row_shr:2 row_mask:0xf bank_mask:0xf
	v_add_f32_dpp v103, v103, v103 row_shr:2 row_mask:0xf bank_mask:0xf
	v_add_f32_dpp v104, v104, v104 row_shr:2 row_mask:0xf bank_mask:0xf
	v_add_f32_dpp v105, v105, v105 row_shr:2 row_mask:0xf bank_mask:0xf
	v_add_f32_dpp v106, v106, v106 row_shr:2 row_mask:0xf bank_mask:0xf
	v_add_f32_dpp v107, v107, v107 row_shr:2 row_mask:0xf bank_mask:0xf
	v_add_f32_dpp v108, v108, v108 row_shr:2 row_mask:0xf bank_mask:0xf
	v_add_f32_dpp v109, v109, v109 row_shr:2 row_mask:0xf bank_mask:0xf
	v_add_f32_dpp v94, v94, v94 row_shr:4 row_mask:0xf bank_mask:0xf
	v_add_f32_dpp v95, v95, v95 row_shr:4 row_mask:0xf bank_mask:0xf
	v_add_f32_dpp v96, v96, v96 row_shr:4 row_mask:0xf bank_mask:0xf
	v_add_f32_dpp v97, v97, v97 row_shr:4 row_mask:0xf bank_mask:0xf
	v_add_f32_dpp v98, v98, v98 row_shr:4 row_mask:0xf bank_mask:0xf
	v_add_f32_dpp v99, v99, v99 row_shr:4 row_mask:0xf bank_mask:0xf
	v_add_f32_dpp v100, v100, v100 row_shr:4 row_mask:0xf bank_mask:0xf
	v_add_f32_dpp v101, v101, v101 row_shr:4 row_mask:0xf bank_mask:0xf
	v_add_f32_dpp v102, v102, v102 row_shr:4 row_mask:0xf bank_mask:0xf
	v_add_f32_dpp v103, v103, v103 row_shr:4 row_mask:0xf bank_mask:0xf
	v_add_f32_dpp v104, v104, v104 row_shr:4 row_mask:0xf bank_mask:0xf
	v_add_f32_dpp v105, v105, v105 row_shr:4 row_mask:0xf bank_mask:0xf
	v_add_f32_dpp v106, v106, v106 row_shr:4 row_mask:0xf bank_mask:0xf
	v_add_f32_dpp v107, v107, v107 row_shr:4 row_mask:0xf bank_mask:0xf
	v_add_f32_dpp v108, v108, v108 row_shr:4 row_mask:0xf bank_mask:0xf
	v_add_f32_dpp v109, v109, v109 row_shr:4 row_mask:0xf bank_mask:0xf
	v_add_f32_dpp v94, v94, v94 row_shr:8 row_mask:0xf bank_mask:0xf
	v_add_f32_dpp v95, v95, v95 row_shr:8 row_mask:0xf bank_mask:0xf
	v_add_f32_dpp v96, v96, v96 row_shr:8 row_mask:0xf bank_mask:0xf
	v_add_f32_dpp v97, v97, v97 row_shr:8 row_mask:0xf bank_mask:0xf
	v_add_f32_dpp v98, v98, v98 row_shr:8 row_mask:0xf bank_mask:0xf
	v_add_f32_dpp v99, v99, v99 row_shr:8 row_mask:0xf bank_mask:0xf
	v_add_f32_dpp v100, v100, v100 row_shr:8 row_mask:0xf bank_mask:0xf
	v_add_f32_dpp v101, v101, v101 row_shr:8 row_mask:0xf bank_mask:0xf
	v_add_f32_dpp v102, v102, v102 row_shr:8 row_mask:0xf bank_mask:0xf
	v_add_f32_dpp v103, v103, v103 row_shr:8 row_mask:0xf bank_mask:0xf
	v_add_f32_dpp v104, v104, v104 row_shr:8 row_mask:0xf bank_mask:0xf
	v_add_f32_dpp v105, v105, v105 row_shr:8 row_mask:0xf bank_mask:0xf
	v_add_f32_dpp v106, v106, v106 row_shr:8 row_mask:0xf bank_mask:0xf
	v_add_f32_dpp v107, v107, v107 row_shr:8 row_mask:0xf bank_mask:0xf
	v_add_f32_dpp v108, v108, v108 row_shr:8 row_mask:0xf bank_mask:0xf
	v_add_f32_dpp v109, v109, v109 row_shr:8 row_mask:0xf bank_mask:0xf
	v_add_f32_dpp v94, v94, v94 row_bcast:15 row_mask:0xa bank_mask:0xf
	v_add_f32_dpp v95, v95, v95 row_bcast:15 row_mask:0xa bank_mask:0xf
	v_add_f32_dpp v96, v96, v96 row_bcast:15 row_mask:0xa bank_mask:0xf
	v_add_f32_dpp v97, v97, v97 row_bcast:15 row_mask:0xa bank_mask:0xf
	v_add_f32_dpp v98, v98, v98 row_bcast:15 row_mask:0xa bank_mask:0xf
	v_add_f32_dpp v99, v99, v99 row_bcast:15 row_mask:0xa bank_mask:0xf
	v_add_f32_dpp v100, v100, v100 row_bcast:15 row_mask:0xa bank_mask:0xf
	v_add_f32_dpp v101, v101, v101 row_bcast:15 row_mask:0xa bank_mask:0xf
	v_add_f32_dpp v102, v102, v102 row_bcast:15 row_mask:0xa bank_mask:0xf
	v_add_f32_dpp v103, v103, v103 row_bcast:15 row_mask:0xa bank_mask:0xf
	v_add_f32_dpp v104, v104, v104 row_bcast:15 row_mask:0xa bank_mask:0xf
	v_add_f32_dpp v105, v105, v105 row_bcast:15 row_mask:0xa bank_mask:0xf
	v_add_f32_dpp v106, v106, v106 row_bcast:15 row_mask:0xa bank_mask:0xf
	v_add_f32_dpp v107, v107, v107 row_bcast:15 row_mask:0xa bank_mask:0xf
	v_add_f32_dpp v108, v108, v108 row_bcast:15 row_mask:0xa bank_mask:0xf
	v_add_f32_dpp v109, v109, v109 row_bcast:15 row_mask:0xa bank_mask:0xf
	s_mov_b32 s46, s28
	s_mov_b32 s47, s29
	s_mov_b64 exec, s[34:35]
	global_store_dword v76, v94, s[46:47]
	s_add_u32 s46, s46, 0x10
	s_addc_u32 s47, s47, 0
	global_store_dword v76, v95, s[46:47]
	s_add_u32 s46, s46, 0x10
	s_addc_u32 s47, s47, 0
	global_store_dword v76, v96, s[46:47]
	s_add_u32 s46, s46, 0x10
	s_addc_u32 s47, s47, 0
	global_store_dword v76, v97, s[46:47]
	s_add_u32 s46, s46, 0x50
	s_addc_u32 s47, s47, 0
	global_store_dword v76, v98, s[46:47]
	s_add_u32 s46, s46, 0x10
	s_addc_u32 s47, s47, 0
	global_store_dword v76, v99, s[46:47]
	s_add_u32 s46, s46, 0x10
	s_addc_u32 s47, s47, 0
	global_store_dword v76, v100, s[46:47]
	s_add_u32 s46, s46, 0x10
	s_addc_u32 s47, s47, 0
	global_store_dword v76, v101, s[46:47]
	s_add_u32 s46, s46, 0x50
	s_addc_u32 s47, s47, 0
	global_store_dword v76, v102, s[46:47]
	s_add_u32 s46, s46, 0x10
	s_addc_u32 s47, s47, 0
	global_store_dword v76, v103, s[46:47]
	s_add_u32 s46, s46, 0x10
	s_addc_u32 s47, s47, 0
	global_store_dword v76, v104, s[46:47]
	s_add_u32 s46, s46, 0x10
	s_addc_u32 s47, s47, 0
	global_store_dword v76, v105, s[46:47]
	s_add_u32 s46, s46, 0x50
	s_addc_u32 s47, s47, 0
	global_store_dword v76, v106, s[46:47]
	s_add_u32 s46, s46, 0x10
	s_addc_u32 s47, s47, 0
	global_store_dword v76, v107, s[46:47]
	s_add_u32 s46, s46, 0x10
	s_addc_u32 s47, s47, 0
	global_store_dword v76, v108, s[46:47]
	s_add_u32 s46, s46, 0x10
	s_addc_u32 s47, s47, 0
	global_store_dword v76, v109, s[46:47]
	s_mov_b64 exec, -1
	s_add_u32 s26, s26, 0x8000
	s_addc_u32 s27, s27, 0
	s_add_u32 s28, s28, 0x200
	s_addc_u32 s29, s29, 0
	v_add_f32_e32 v159, 0x42000000, v159
	s_add_i32 s30, s30, 1
	s_waitcnt vmcnt(48)
	s_cmp_lt_u32 s30, 4
	s_cbranch_scc1 .Lhfc_blk
	s_mov_b64 s[4:5], 0
	s_barrier
